# v034 + topk: mono() as v_ashrrev + v_bitop3 (x ^ ((x>>31) | 0x80000000)) instead of v_cmp + v_cndmask + v_xor at 55 sites
# speedup vs baseline: 1.0119x; 1.0032x over previous
; #define LAS __attribute__((address_space(3)))
; __device__ __forceinline__ f32x4 mfma16(bf16x8 a, bf16x8 b, f32x4 c) { return __builtin_amdgcn_mfma_f32_16x16x32_bf16(a, b, c, 0, 0, 0); }
; __device__ __forceinline__ void topk_phase(LAS unsigned char* lds, const bf16_t* qp, const bf16_t* keys, const float* SU, const float* SV, int* sel_e, float* sel_g, float* sel_su, int G, int b) {
;     ...
;         const int tt = gu.pm * 2 + (ui & 1), h = gu.pn;
;         const int tok = tt * 128 + wid * 16 + fr;
;         if ((ui & 1) == 0) {
;             if (ui == 0) {
;                 const bf16_t* src = keys + (size_t)h * 2 * 16384 + (size_t)krow * 128 + khf * 64;
; #pragma unroll
;                 for (int q8 = 0; q8 < 8; ++q8) kpre[q8] = *(const u32x4*)(src + q8 * 8);
;             } else __syncthreads();
;             LAS bf16_t* dst = KL + krow * 136 + khf * 64;
; #pragma unroll
;             for (int q8 = 0; q8 < 8; ++q8) *(LAS u32x4*)(dst + q8 * 8) = kpre[q8];
;             __syncthreads();
;         } else {
;             pg8::Unit gn;
;             if (SO.next((ui + 1) >> 1, gn)) { const bf16_t* src = keys + (size_t)gn.pn * 2 * 16384 + (size_t)krow * 128 + khf * 64;
; #pragma unroll
;                 for (int q8 = 0; q8 < 8; ++q8) kpre[q8] = *(const u32x4*)(src + q8 * 8); }
;         }
;         unsigned T[2][16];
; #pragma unroll
;         for (int p = 0; p < 2; ++p) {
;             f32x4 acc[8];
; #pragma unroll
;             for (int mt = 0; mt < 8; ++mt) acc[mt] = (f32x4){0.f, 0.f, 0.f, 0.f};
;             bf16x8 bq[4];
; #pragma unroll
;             for (int ks = 0; ks < 4; ++ks) bq[ks] = *(const bf16x8*)(qp + (size_t)tok * D_ + h * 256 + p * 128 + ks * 32 + fq * 8);
;             const LAS bf16_t* kb = KL + p * 128 * 136;
; #pragma unroll
;             for (int mt = 0; mt < 8; ++mt)
; #pragma unroll
;                 for (int ks = 0; ks < 4; ++ks) { const bf16x8 a = *(const LAS bf16x8*)(kb + (mt * 16 + fr) * 136 + ks * 32 + fq * 8); acc[mt] = mfma16(a, bq[ks], acc[mt]); }
.LBB0_659:
	s_and_b32 s0, s52, 1
	s_lshl_b32 s1, s64, 8
	s_lshl_b32 s0, s0, 7
	s_or_b32 s0, s1, s0
	v_add_u32_e32 v94, s0, v85
	v_ashrrev_i32_e32 v95, 31, v94
	v_lshlrev_b64 v[34:35], 12, v[94:95]
	s_lshl_b32 s0, s56, 8
	v_lshl_add_u64 v[34:35], s[74:75], 0, v[34:35]
	s_ashr_i32 s1, s0, 31
	v_lshl_add_u64 v[34:35], s[0:1], 1, v[34:35]
	v_lshl_add_u64 v[96:97], v[34:35], 0, v[78:79]
	global_load_dwordx4 v[66:69], v[96:97], off
	global_load_dwordx4 v[62:65], v[96:97], off offset:64
	global_load_dwordx4 v[58:61], v[96:97], off offset:128
	global_load_dwordx4 v[54:57], v[96:97], off offset:192
	v_add_u32_e32 v138, v87, v89
	ds_read_b128 v[34:37], v138 offset:32768
	ds_read_b128 v[38:41], v138 offset:32832
	s_movk_i32 s0, 0xff
	s_waitcnt vmcnt(3) lgkmcnt(1)
	v_mfma_f32_16x16x32_bf16 v[34:37], v[34:37], v[66:69], 0
	ds_read_b128 v[42:45], v138 offset:41536
	ds_read_b128 v[50:53], v138 offset:45888
	ds_read_b128 v[70:73], v138 offset:50240
	s_waitcnt vmcnt(2) lgkmcnt(3)
	v_mfma_f32_16x16x32_bf16 v[34:37], v[38:41], v[62:65], v[34:37]
	ds_read_b128 v[38:41], v138 offset:32896
	ds_read_b128 v[74:77], v138 offset:54592
	ds_read_b128 v[134:137], v138 offset:58944
	s_waitcnt vmcnt(1) lgkmcnt(2)
	v_mfma_f32_16x16x32_bf16 v[34:37], v[38:41], v[58:61], v[34:37]
	ds_read_b128 v[38:41], v138 offset:32960
	s_waitcnt vmcnt(0) lgkmcnt(0)
	v_mfma_f32_16x16x32_bf16 v[46:49], v[38:41], v[54:57], v[34:37]
	s_nop 4
	ds_read_b128 v[34:37], v138 offset:37120
	ds_read_b128 v[38:41], v138 offset:37184
	s_nop 0
	s_waitcnt lgkmcnt(1)
	v_mfma_f32_16x16x32_bf16 v[34:37], v[34:37], v[66:69], 0
	s_waitcnt lgkmcnt(0)
	v_mfma_f32_16x16x32_bf16 v[34:37], v[38:41], v[62:65], v[34:37]
	ds_read_b128 v[38:41], v138 offset:37248
	s_waitcnt lgkmcnt(0)
	v_mfma_f32_16x16x32_bf16 v[34:37], v[38:41], v[58:61], v[34:37]
	ds_read_b128 v[38:41], v138 offset:37312
	s_waitcnt lgkmcnt(0)
	v_mfma_f32_16x16x32_bf16 v[34:37], v[38:41], v[54:57], v[34:37]
	ds_read_b128 v[38:41], v138 offset:41472
	s_waitcnt lgkmcnt(0)
	v_mfma_f32_16x16x32_bf16 v[38:41], v[38:41], v[66:69], 0
	v_mfma_f32_16x16x32_bf16 v[38:41], v[42:45], v[62:65], v[38:41]
	ds_read_b128 v[42:45], v138 offset:41600
	s_waitcnt lgkmcnt(0)
	v_mfma_f32_16x16x32_bf16 v[38:41], v[42:45], v[58:61], v[38:41]
	ds_read_b128 v[42:45], v138 offset:41664
	s_waitcnt lgkmcnt(0)
	v_mfma_f32_16x16x32_bf16 v[38:41], v[42:45], v[54:57], v[38:41]
	ds_read_b128 v[42:45], v138 offset:45824
	s_waitcnt lgkmcnt(0)
	v_mfma_f32_16x16x32_bf16 v[42:45], v[42:45], v[66:69], 0
	v_mfma_f32_16x16x32_bf16 v[42:45], v[50:53], v[62:65], v[42:45]
	ds_read_b128 v[50:53], v138 offset:45952
	s_waitcnt lgkmcnt(0)
	v_mfma_f32_16x16x32_bf16 v[42:45], v[50:53], v[58:61], v[42:45]
	ds_read_b128 v[50:53], v138 offset:46016
	s_waitcnt lgkmcnt(0)
	v_mfma_f32_16x16x32_bf16 v[42:45], v[50:53], v[54:57], v[42:45]
	ds_read_b128 v[50:53], v138 offset:50176
	s_waitcnt lgkmcnt(0)
	v_mfma_f32_16x16x32_bf16 v[50:53], v[50:53], v[66:69], 0
	v_mfma_f32_16x16x32_bf16 v[50:53], v[70:73], v[62:65], v[50:53]
	ds_read_b128 v[70:73], v138 offset:50304
	s_waitcnt lgkmcnt(0)
	v_mfma_f32_16x16x32_bf16 v[50:53], v[70:73], v[58:61], v[50:53]
	ds_read_b128 v[70:73], v138 offset:50368
	s_waitcnt lgkmcnt(0)
	v_mfma_f32_16x16x32_bf16 v[70:73], v[70:73], v[54:57], v[50:53]
	s_nop 4
	ds_read_b128 v[50:53], v138 offset:54528
	s_waitcnt lgkmcnt(0)
	v_mfma_f32_16x16x32_bf16 v[50:53], v[50:53], v[66:69], 0
	v_mfma_f32_16x16x32_bf16 v[50:53], v[74:77], v[62:65], v[50:53]
	ds_read_b128 v[74:77], v138 offset:54656
	s_waitcnt lgkmcnt(0)
	v_mfma_f32_16x16x32_bf16 v[50:53], v[74:77], v[58:61], v[50:53]
	ds_read_b128 v[74:77], v138 offset:54720
	s_waitcnt lgkmcnt(0)
	v_mfma_f32_16x16x32_bf16 v[50:53], v[74:77], v[54:57], v[50:53]
	ds_read_b128 v[74:77], v138 offset:58880
	s_waitcnt lgkmcnt(0)
	v_mfma_f32_16x16x32_bf16 v[74:77], v[74:77], v[66:69], 0
	v_mfma_f32_16x16x32_bf16 v[74:77], v[134:137], v[62:65], v[74:77]
	ds_read_b128 v[134:137], v138 offset:59008
	s_waitcnt lgkmcnt(0)
	v_mfma_f32_16x16x32_bf16 v[74:77], v[134:137], v[58:61], v[74:77]
	ds_read_b128 v[134:137], v138 offset:59072
	s_waitcnt lgkmcnt(0)
	v_mfma_f32_16x16x32_bf16 v[74:77], v[134:137], v[54:57], v[74:77]
	ds_read_b128 v[134:137], v138 offset:63232
	s_waitcnt lgkmcnt(0)
	v_mfma_f32_16x16x32_bf16 v[66:69], v[134:137], v[66:69], 0
	ds_read_b128 v[134:137], v138 offset:63296
	s_waitcnt lgkmcnt(0)
	v_mfma_f32_16x16x32_bf16 v[62:65], v[134:137], v[62:65], v[66:69]
	s_nop 4
	ds_read_b128 v[66:69], v138 offset:63360
	s_waitcnt lgkmcnt(0)
	v_mfma_f32_16x16x32_bf16 v[58:61], v[66:69], v[58:61], v[62:65]
	s_nop 2
	ds_read_b128 v[62:65], v138 offset:63424
	s_waitcnt lgkmcnt(0)
; __device__ __forceinline__ unsigned mono(float f) { const unsigned u = __float_as_uint(f); return (u & 0x80000000u) ? ~u : (u ^ 0x80000000u); }
; __device__ __forceinline__ void topk_phase(LAS unsigned char* lds, const bf16_t* qp, const bf16_t* keys, const float* SU, const float* SV, int* sel_e, float* sel_g, float* sel_su, int G, int b) {
;     ...
;             unsigned lo16[16];
; #pragma unroll
;             for (int mt = 0; mt < 4; ++mt)
; #pragma unroll
;                 for (int r = 0; r < 4; ++r) {
;                     T[p][mt * 4 + r] = (mono(acc[mt][r]) & ~127u) | (unsigned)(127 - (mt * 16 + fq * 4 + r));
;                     lo16[mt * 4 + r] = (mono(acc[mt + 4][r]) & ~127u) | (unsigned)(127 - ((mt + 4) * 16 + fq * 4 + r));
;                 }
;             SN_SORT16(T[p]); SN_SORT16(lo16);
	v_mfma_f32_16x16x32_bf16 v[54:57], v[62:65], v[54:57], v[58:61]
	s_nop 2
	v_ashrrev_i32_e32 v58, 31, v46
	v_bitop3_b32 v46, v46, v58, v132 bitop3:0x1e
	v_and_or_b32 v46, v46, s53, v98
	v_ashrrev_i32_e32 v58, 31, v70
	v_bitop3_b32 v58, v70, v58, v132 bitop3:0x1e
	v_and_or_b32 v58, v58, s53, v99
	v_ashrrev_i32_e32 v59, 31, v47
	v_bitop3_b32 v47, v47, v59, v132 bitop3:0x1e
	v_and_or_b32 v47, v47, s53, v100
	v_ashrrev_i32_e32 v59, 31, v71
	v_bitop3_b32 v59, v71, v59, v132 bitop3:0x1e
	v_and_or_b32 v59, v59, s53, v101
	v_ashrrev_i32_e32 v60, 31, v48
	v_bitop3_b32 v48, v48, v60, v132 bitop3:0x1e
	v_and_or_b32 v48, v48, s53, v102
	v_ashrrev_i32_e32 v60, 31, v72
	v_bitop3_b32 v60, v72, v60, v132 bitop3:0x1e
	v_and_or_b32 v60, v60, s53, v103
	v_ashrrev_i32_e32 v61, 31, v49
	v_bitop3_b32 v49, v49, v61, v132 bitop3:0x1e
	v_and_or_b32 v49, v49, s53, v104
	v_ashrrev_i32_e32 v61, 31, v73
	v_bitop3_b32 v61, v73, v61, v132 bitop3:0x1e
	v_and_or_b32 v61, v61, s53, v105
	v_ashrrev_i32_e32 v62, 31, v34
	v_bitop3_b32 v34, v34, v62, v132 bitop3:0x1e
	v_and_or_b32 v34, v34, s53, v106
	v_ashrrev_i32_e32 v62, 31, v50
	v_bitop3_b32 v50, v50, v62, v132 bitop3:0x1e
	v_and_or_b32 v50, v50, s53, v107
	v_ashrrev_i32_e32 v62, 31, v35
	v_bitop3_b32 v35, v35, v62, v132 bitop3:0x1e
	v_and_or_b32 v35, v35, s53, v108
	v_ashrrev_i32_e32 v62, 31, v51
	v_bitop3_b32 v51, v51, v62, v132 bitop3:0x1e
	v_and_or_b32 v51, v51, s53, v109
	v_ashrrev_i32_e32 v62, 31, v36
	v_bitop3_b32 v36, v36, v62, v132 bitop3:0x1e
	v_and_or_b32 v36, v36, s53, v110
	v_ashrrev_i32_e32 v62, 31, v52
	v_bitop3_b32 v52, v52, v62, v132 bitop3:0x1e
	v_and_or_b32 v52, v52, s53, v111
	v_ashrrev_i32_e32 v62, 31, v37
	v_bitop3_b32 v37, v37, v62, v132 bitop3:0x1e
	v_and_or_b32 v37, v37, s53, v112
	v_ashrrev_i32_e32 v62, 31, v53
	v_bitop3_b32 v53, v53, v62, v132 bitop3:0x1e
	v_and_or_b32 v53, v53, s53, v113
	v_ashrrev_i32_e32 v62, 31, v38
	v_bitop3_b32 v38, v38, v62, v132 bitop3:0x1e
	v_and_or_b32 v38, v38, s53, v114
	v_ashrrev_i32_e32 v62, 31, v74
	v_bitop3_b32 v62, v74, v62, v132 bitop3:0x1e
	v_max_u32_e32 v74, v58, v59
	v_ashrrev_i32_e32 v63, 31, v39
	v_cmp_lt_i32_e32 vcc, -1, v75
	v_bitop3_b32 v39, v39, v63, v132 bitop3:0x1e
	v_min_u32_e32 v58, v58, v59
	v_cndmask_b32_e32 v63, -1, v132, vcc
	v_max_u32_e32 v59, v60, v61
	v_min_u32_e32 v60, v60, v61
	v_ashrrev_i32_e32 v64, 31, v40
	v_cmp_lt_i32_e32 vcc, -1, v76
	v_bitop3_b32 v40, v40, v64, v132 bitop3:0x1e
	v_max_u32_e32 v61, v74, v59
	v_cndmask_b32_e32 v64, -1, v132, vcc
	v_min_u32_e32 v59, v74, v59
	v_max_u32_e32 v74, v58, v60
	v_ashrrev_i32_e32 v65, 31, v41
	v_cmp_lt_i32_e32 vcc, -1, v77
	v_bitop3_b32 v41, v41, v65, v132 bitop3:0x1e
	v_min_u32_e32 v58, v58, v60
	v_cndmask_b32_e32 v65, -1, v132, vcc
	v_max_u32_e32 v60, v74, v59
	v_min_u32_e32 v59, v74, v59
	v_ashrrev_i32_e32 v66, 31, v42
	v_bitop3_b32 v42, v42, v66, v132 bitop3:0x1e
	v_max_u32_e32 v74, v50, v51
	v_ashrrev_i32_e32 v66, 31, v54
	v_bitop3_b32 v54, v54, v66, v132 bitop3:0x1e
	v_min_u32_e32 v50, v50, v51
	v_ashrrev_i32_e32 v66, 31, v43
	v_bitop3_b32 v43, v43, v66, v132 bitop3:0x1e
	v_max_u32_e32 v51, v52, v53
	v_ashrrev_i32_e32 v66, 31, v55
	v_bitop3_b32 v55, v55, v66, v132 bitop3:0x1e
	v_min_u32_e32 v52, v52, v53
	v_ashrrev_i32_e32 v66, 31, v44
	v_bitop3_b32 v44, v44, v66, v132 bitop3:0x1e
	v_max_u32_e32 v53, v74, v51
	v_ashrrev_i32_e32 v66, 31, v56
	v_bitop3_b32 v56, v56, v66, v132 bitop3:0x1e
	v_min_u32_e32 v51, v74, v51
	v_ashrrev_i32_e32 v66, 31, v45
	v_cmp_lt_i32_e32 vcc, -1, v57
	v_bitop3_b32 v45, v45, v66, v132 bitop3:0x1e
	v_max_u32_e32 v74, v50, v52
	v_cndmask_b32_e32 v66, -1, v132, vcc
	v_xor_b32_e32 v57, v66, v57
	v_max_u32_e32 v66, v46, v47
	v_min_u32_e32 v46, v46, v47
	v_max_u32_e32 v47, v48, v49
	v_min_u32_e32 v48, v48, v49
	v_max_u32_e32 v49, v66, v47
	v_min_u32_e32 v47, v66, v47
	v_max_u32_e32 v66, v46, v48
	v_min_u32_e32 v46, v46, v48
	v_max_u32_e32 v48, v66, v47
	v_min_u32_e32 v47, v66, v47
	v_max_u32_e32 v66, v34, v35
	v_min_u32_e32 v34, v34, v35
	v_max_u32_e32 v35, v36, v37
	v_min_u32_e32 v36, v36, v37
	v_max_u32_e32 v37, v66, v35
	v_min_u32_e32 v35, v66, v35
	v_max_u32_e32 v66, v34, v36
	v_min_u32_e32 v34, v34, v36
	v_max_u32_e32 v36, v66, v35
	v_min_u32_e32 v35, v66, v35
	v_min_u32_e32 v50, v50, v52
	v_max_u32_e32 v52, v74, v51
	v_min_u32_e32 v51, v74, v51
	v_max_u32_e32 v66, v49, v37
	v_min_u32_e32 v37, v49, v37
	v_max_u32_e32 v49, v47, v35
	v_max_u32_e32 v74, v61, v53
	v_min_u32_e32 v53, v61, v53
	v_max_u32_e32 v61, v59, v51
	v_xor_b32_e32 v63, v63, v75
	v_xor_b32_e32 v64, v64, v76
	v_xor_b32_e32 v65, v65, v77
	v_min_u32_e32 v35, v47, v35
	v_max_u32_e32 v47, v49, v37
	v_min_u32_e32 v37, v49, v37
	v_max_u32_e32 v49, v48, v36
	v_min_u32_e32 v36, v48, v36
	v_max_u32_e32 v48, v46, v34
	v_min_u32_e32 v51, v59, v51
	v_max_u32_e32 v59, v61, v53
	v_min_u32_e32 v53, v61, v53
	v_max_u32_e32 v61, v60, v52
	v_min_u32_e32 v52, v60, v52
	v_max_u32_e32 v60, v58, v50
	v_and_or_b32 v62, v62, s53, v115
	v_and_or_b32 v39, v39, s53, v116
	v_and_or_b32 v63, v63, s53, v117
	v_and_or_b32 v40, v40, s53, v118
	v_and_or_b32 v64, v64, s53, v119
	v_and_or_b32 v41, v41, s53, v120
	v_and_or_b32 v65, v65, s53, v121
	v_min_u32_e32 v34, v46, v34
	v_max_u32_e32 v46, v48, v36
	v_min_u32_e32 v36, v48, v36
	v_min_u32_e32 v50, v58, v50
	v_max_u32_e32 v58, v60, v52
	v_min_u32_e32 v52, v60, v52
	v_max_u32_e32 v48, v49, v47
	v_min_u32_e32 v47, v49, v47
	v_max_u32_e32 v49, v46, v37
	v_min_u32_e32 v37, v46, v37
	v_max_u32_e32 v46, v36, v35
	v_min_u32_e32 v35, v36, v35
	v_max_u32_e32 v36, v38, v39
	v_min_u32_e32 v38, v38, v39
	v_max_u32_e32 v39, v40, v41
	v_min_u32_e32 v40, v40, v41
	v_max_u32_e32 v60, v61, v59
; __device__ __forceinline__ void topk_phase(LAS unsigned char* lds, const bf16_t* qp, const bf16_t* keys, const float* SU, const float* SV, int* sel_e, float* sel_g, float* sel_su, int G, int b) {
;     ...
;             SN_SORT16(T[p]); SN_SORT16(lo16);
; #pragma unroll
;             for (int i = 0; i < 16; ++i) T[p][i] = umax_(T[p][i], lo16[15 - i]);
;             SN_BITONIC16(T[p]);
	v_min_u32_e32 v59, v61, v59
	v_max_u32_e32 v61, v58, v53
	v_min_u32_e32 v53, v58, v53
	v_max_u32_e32 v58, v52, v51
	v_min_u32_e32 v51, v52, v51
	v_max_u32_e32 v52, v62, v63
	v_min_u32_e32 v62, v62, v63
	v_max_u32_e32 v63, v64, v65
	v_min_u32_e32 v64, v64, v65
	v_and_or_b32 v42, v42, s53, v122
	v_and_or_b32 v54, v54, s53, v123
	v_and_or_b32 v43, v43, s53, v124
	v_and_or_b32 v55, v55, s53, v125
	v_and_or_b32 v44, v44, s53, v126
	v_and_or_b32 v56, v56, s53, v127
	v_and_or_b32 v45, v45, s53, v128
	v_and_or_b32 v57, v57, s53, v129
	v_max_u32_e32 v41, v36, v39
	v_min_u32_e32 v36, v36, v39
	v_max_u32_e32 v39, v38, v40
	v_max_u32_e32 v65, v52, v63
	v_min_u32_e32 v52, v52, v63
	v_max_u32_e32 v63, v62, v64
	v_min_u32_e32 v38, v38, v40
	v_max_u32_e32 v40, v39, v36
	v_min_u32_e32 v36, v39, v36
	v_max_u32_e32 v39, v42, v43
	v_min_u32_e32 v42, v42, v43
	v_max_u32_e32 v43, v44, v45
	v_min_u32_e32 v44, v44, v45
	v_min_u32_e32 v62, v62, v64
	v_max_u32_e32 v64, v63, v52
	v_min_u32_e32 v52, v63, v52
	v_max_u32_e32 v63, v54, v55
	v_min_u32_e32 v54, v54, v55
	v_max_u32_e32 v55, v56, v57
	v_min_u32_e32 v56, v56, v57
	v_max_u32_e32 v45, v39, v43
	v_min_u32_e32 v39, v39, v43
	v_max_u32_e32 v43, v42, v44
	v_max_u32_e32 v57, v63, v55
	v_min_u32_e32 v55, v63, v55
	v_max_u32_e32 v63, v54, v56
	v_min_u32_e32 v42, v42, v44
	v_max_u32_e32 v44, v43, v39
	v_min_u32_e32 v39, v43, v39
	v_min_u32_e32 v54, v54, v56
	v_max_u32_e32 v56, v63, v55
	v_min_u32_e32 v55, v63, v55
	v_max_u32_e32 v43, v41, v45
	v_min_u32_e32 v41, v41, v45
	v_max_u32_e32 v45, v36, v39
	v_max_u32_e32 v63, v65, v57
	v_min_u32_e32 v57, v65, v57
	v_max_u32_e32 v65, v52, v55
	v_min_u32_e32 v36, v36, v39
	v_max_u32_e32 v39, v45, v41
	v_min_u32_e32 v41, v45, v41
	v_max_u32_e32 v45, v40, v44
	v_min_u32_e32 v40, v40, v44
	v_max_u32_e32 v44, v38, v42
	v_min_u32_e32 v52, v52, v55
	v_max_u32_e32 v55, v65, v57
	v_min_u32_e32 v57, v65, v57
	v_max_u32_e32 v65, v64, v56
	v_min_u32_e32 v56, v64, v56
	v_max_u32_e32 v64, v62, v54
	v_min_u32_e32 v38, v38, v42
	v_max_u32_e32 v42, v44, v40
	v_min_u32_e32 v54, v62, v54
	v_max_u32_e32 v62, v64, v56
	v_min_u32_e32 v40, v44, v40
	v_max_u32_e32 v44, v45, v39
	v_min_u32_e32 v39, v45, v39
	v_max_u32_e32 v45, v42, v41
	v_min_u32_e32 v41, v42, v41
	v_min_u32_e32 v56, v64, v56
	v_max_u32_e32 v64, v65, v55
	v_min_u32_e32 v55, v65, v55
	v_max_u32_e32 v65, v62, v57
	v_min_u32_e32 v57, v62, v57
	v_max_u32_e32 v42, v40, v36
	v_min_u32_e32 v36, v40, v36
	v_min_u32_e32 v40, v66, v43
	v_max_u32_e32 v67, v37, v41
	v_max_u32_e32 v62, v56, v52
	v_min_u32_e32 v52, v56, v52
	v_min_u32_e32 v56, v74, v63
	v_max_u32_e32 v75, v53, v57
	v_min_u32_e32 v37, v37, v41
	v_max_u32_e32 v41, v67, v40
	v_min_u32_e32 v40, v67, v40
	v_max_u32_e32 v67, v47, v39
	v_min_u32_e32 v39, v47, v39
	v_max_u32_e32 v47, v35, v36
	v_min_u32_e32 v53, v53, v57
	v_max_u32_e32 v57, v75, v56
	v_min_u32_e32 v56, v75, v56
	v_max_u32_e32 v75, v59, v55
	v_min_u32_e32 v55, v59, v55
	v_max_u32_e32 v59, v51, v52
	v_min_u32_e32 v35, v35, v36
	v_max_u32_e32 v36, v47, v39
	v_min_u32_e32 v39, v47, v39
	v_min_u32_e32 v51, v51, v52
	v_max_u32_e32 v52, v59, v55
	v_min_u32_e32 v55, v59, v55
	v_max_u32_e32 v47, v67, v41
	v_min_u32_e32 v41, v67, v41
	v_max_u32_e32 v67, v36, v40
	v_min_u32_e32 v36, v36, v40
	v_max_u32_e32 v40, v39, v37
	v_min_u32_e32 v37, v39, v37
	v_max_u32_e32 v39, v48, v44
	v_min_u32_e32 v44, v48, v44
	v_max_u32_e32 v48, v46, v42
	v_max_u32_e32 v59, v75, v57
	v_min_u32_e32 v57, v75, v57
	v_max_u32_e32 v75, v52, v56
	v_min_u32_e32 v52, v52, v56
	v_max_u32_e32 v56, v55, v53
	v_min_u32_e32 v53, v55, v53
	v_max_u32_e32 v55, v60, v64
	v_min_u32_e32 v60, v60, v64
	v_max_u32_e32 v64, v58, v62
	v_min_u32_e32 v42, v46, v42
	v_max_u32_e32 v46, v48, v44
	v_min_u32_e32 v44, v48, v44
	v_max_u32_e32 v48, v49, v45
	v_min_u32_e32 v45, v49, v45
	v_max_u32_e32 v49, v34, v38
	v_min_u32_e32 v58, v58, v62
	v_max_u32_e32 v62, v64, v60
	v_min_u32_e32 v60, v64, v60
	v_max_u32_e32 v64, v61, v65
	v_min_u32_e32 v61, v61, v65
	v_max_u32_e32 v65, v50, v54
	v_min_u32_e32 v34, v34, v38
	v_max_u32_e32 v38, v49, v45
	v_min_u32_e32 v45, v49, v45
	v_min_u32_e32 v50, v50, v54
	v_max_u32_e32 v54, v65, v61
	v_min_u32_e32 v61, v65, v61
	v_max_u32_e32 v49, v48, v46
	v_min_u32_e32 v46, v48, v46
	v_max_u32_e32 v48, v38, v44
	v_min_u32_e32 v38, v38, v44
	v_max_u32_e32 v44, v45, v42
	v_min_u32_e32 v42, v45, v42
	v_max_u32_e32 v65, v64, v62
	v_min_u32_e32 v62, v64, v62
	v_max_u32_e32 v64, v54, v60
	v_min_u32_e32 v54, v54, v60
	v_max_u32_e32 v60, v61, v58
	v_min_u32_e32 v58, v61, v58
	v_min_u32_e32 v45, v39, v47
	v_min_u32_e32 v68, v49, v41
	v_min_u32_e32 v69, v46, v67
	v_min_u32_e32 v70, v48, v36
	v_min_u32_e32 v71, v38, v40
	v_min_u32_e32 v72, v44, v37
	v_min_u32_e32 v73, v42, v35
	v_min_u32_e32 v61, v55, v59
	v_min_u32_e32 v76, v65, v57
	v_min_u32_e32 v77, v62, v75
	v_min_u32_e32 v134, v64, v52
	v_min_u32_e32 v135, v54, v56
	v_min_u32_e32 v136, v60, v53
	v_min_u32_e32 v137, v58, v51
	v_max3_u32 v43, v66, v43, v50
	v_max3_u32 v39, v39, v47, v137
	v_max3_u32 v45, v45, v58, v51
	v_max3_u32 v41, v49, v41, v136
	v_max3_u32 v47, v68, v60, v53
	v_max3_u32 v46, v46, v67, v135
	v_max3_u32 v49, v69, v54, v56
	v_max3_u32 v36, v48, v36, v134
	v_max3_u32 v48, v70, v64, v52
	v_max3_u32 v38, v38, v40, v77
	v_max3_u32 v40, v71, v62, v75
	v_max3_u32 v37, v44, v37, v76
	v_max3_u32 v44, v72, v65, v57
	v_max3_u32 v35, v42, v35, v61
	v_max3_u32 v42, v73, v55, v59
	v_max3_u32 v34, v34, v74, v63
	v_max_u32_e32 v50, v43, v48
	v_min_u32_e32 v43, v43, v48
	v_max_u32_e32 v48, v39, v38
	v_min_u32_e32 v38, v39, v38
	v_max_u32_e32 v39, v45, v40
	v_min_u32_e32 v40, v45, v40
	v_max_u32_e32 v45, v41, v37
; #define LAS __attribute__((address_space(3)))
; __device__ __forceinline__ f32x4 mfma16(bf16x8 a, bf16x8 b, f32x4 c) { return __builtin_amdgcn_mfma_f32_16x16x32_bf16(a, b, c, 0, 0, 0); }
; __device__ __forceinline__ void topk_phase(LAS unsigned char* lds, const bf16_t* qp, const bf16_t* keys, const float* SU, const float* SV, int* sel_e, float* sel_g, float* sel_su, int G, int b) {
;     ...
;             bf16x8 bq[4];
; #pragma unroll
;             for (int ks = 0; ks < 4; ++ks) bq[ks] = *(const bf16x8*)(qp + (size_t)tok * D_ + h * 256 + p * 128 + ks * 32 + fq * 8);
;             const LAS bf16_t* kb = KL + p * 128 * 136;
; #pragma unroll
;             for (int mt = 0; mt < 8; ++mt)
; #pragma unroll
;                 for (int ks = 0; ks < 4; ++ks) { const bf16x8 a = *(const LAS bf16x8*)(kb + (mt * 16 + fr) * 136 + ks * 32 + fq * 8); acc[mt] = mfma16(a, bq[ks], acc[mt]); }
	v_min_u32_e32 v37, v41, v37
	v_max_u32_e32 v41, v47, v44
	v_min_u32_e32 v44, v47, v44
	v_max_u32_e32 v47, v46, v35
	v_min_u32_e32 v35, v46, v35
	v_max_u32_e32 v46, v49, v42
	v_min_u32_e32 v42, v49, v42
	v_max_u32_e32 v49, v36, v34
	v_min_u32_e32 v34, v36, v34
	v_max_u32_e32 v36, v50, v41
	v_min_u32_e32 v41, v50, v41
	v_max_u32_e32 v50, v48, v47
	v_min_u32_e32 v47, v48, v47
	v_max_u32_e32 v48, v39, v46
	v_min_u32_e32 v39, v39, v46
	v_max_u32_e32 v46, v45, v49
	v_min_u32_e32 v45, v45, v49
	v_max_u32_e32 v49, v43, v44
	v_min_u32_e32 v43, v43, v44
	v_max_u32_e32 v44, v38, v35
	v_min_u32_e32 v35, v38, v35
	v_max_u32_e32 v38, v40, v42
	v_min_u32_e32 v40, v40, v42
	v_max_u32_e32 v42, v37, v34
	v_min_u32_e32 v34, v37, v34
	v_max_u32_e32 v37, v36, v48
	v_min_u32_e32 v36, v36, v48
	v_max_u32_e32 v48, v50, v46
	v_min_u32_e32 v46, v50, v46
	v_max_u32_e32 v50, v41, v39
	v_min_u32_e32 v39, v41, v39
	v_max_u32_e32 v41, v47, v45
	v_min_u32_e32 v45, v47, v45
	v_max_u32_e32 v47, v49, v38
	v_min_u32_e32 v38, v49, v38
	v_max_u32_e32 v49, v44, v42
	v_min_u32_e32 v42, v44, v42
	v_max_u32_e32 v44, v43, v40
	v_min_u32_e32 v40, v43, v40
	v_max_u32_e32 v43, v35, v34
	v_min_u32_e32 v34, v35, v34
	v_max_u32_e32 v35, v37, v48
	v_min_u32_e32 v37, v37, v48
	v_max_u32_e32 v48, v36, v46
	v_min_u32_e32 v36, v36, v46
	v_max_u32_e32 v46, v50, v41
	v_min_u32_e32 v41, v50, v41
	v_max_u32_e32 v50, v39, v45
	v_min_u32_e32 v39, v39, v45
	v_max_u32_e32 v45, v47, v49
	v_min_u32_e32 v47, v47, v49
	v_max_u32_e32 v49, v38, v42
	v_min_u32_e32 v38, v38, v42
	v_max_u32_e32 v42, v44, v43
	v_min_u32_e32 v43, v44, v43
	v_max_u32_e32 v44, v40, v34
	v_min_u32_e32 v34, v40, v34
	v_mov_b32_e32 v40, v35
	v_mov_b32_e32 v51, v37
	v_mov_b32_e32 v52, v48
	v_mov_b32_e32 v53, v36
	v_mov_b32_e32 v54, v46
	v_mov_b32_e32 v55, v41
	v_mov_b32_e32 v56, v50
	v_mov_b32_e32 v57, v39
	v_mov_b32_e32 v58, v45
	v_mov_b32_e32 v59, v47
	v_mov_b32_e32 v60, v49
	v_mov_b32_e32 v61, v38
	v_mov_b32_e32 v62, v42
	v_mov_b32_e32 v63, v43
	v_mov_b32_e32 v64, v44
	v_mov_b32_e32 v65, v34
	v_permlane16_swap_b32_e32 v35, v40
	v_permlane16_swap_b32_e32 v37, v51
	v_permlane16_swap_b32_e32 v48, v52
	v_permlane16_swap_b32_e32 v36, v53
	v_permlane16_swap_b32_e32 v46, v54
	v_permlane16_swap_b32_e32 v41, v55
	v_permlane16_swap_b32_e32 v50, v56
	v_permlane16_swap_b32_e32 v39, v57
	v_permlane16_swap_b32_e32 v45, v58
	v_permlane16_swap_b32_e32 v47, v59
	v_permlane16_swap_b32_e32 v49, v60
	v_permlane16_swap_b32_e32 v38, v61
	v_permlane16_swap_b32_e32 v42, v62
	v_permlane16_swap_b32_e32 v43, v63
	v_permlane16_swap_b32_e32 v44, v64
	v_permlane16_swap_b32_e32 v34, v65
	v_max_u32_e32 v35, v35, v65
	v_max_u32_e32 v37, v37, v64
	v_max_u32_e32 v48, v48, v63
	v_max_u32_e32 v36, v36, v62
	v_max_u32_e32 v46, v46, v61
	v_max_u32_e32 v41, v41, v60
	v_max_u32_e32 v50, v50, v59
	v_max_u32_e32 v39, v39, v58
	v_max_u32_e32 v45, v45, v57
	v_max_u32_e32 v47, v47, v56
	v_max_u32_e32 v49, v49, v55
	v_max_u32_e32 v38, v38, v54
	v_max_u32_e32 v42, v42, v53
	v_max_u32_e32 v43, v43, v52
	v_max_u32_e32 v44, v44, v51
	v_max_u32_e32 v34, v34, v40
	v_max_u32_e32 v40, v35, v45
	v_min_u32_e32 v35, v35, v45
	v_max_u32_e32 v45, v37, v47
	v_min_u32_e32 v37, v37, v47
	v_max_u32_e32 v47, v48, v49
	v_min_u32_e32 v48, v48, v49
	v_max_u32_e32 v49, v36, v38
	v_min_u32_e32 v36, v36, v38
	v_max_u32_e32 v38, v46, v42
	v_min_u32_e32 v42, v46, v42
	v_max_u32_e32 v46, v41, v43
	v_min_u32_e32 v41, v41, v43
	v_max_u32_e32 v43, v50, v44
	v_min_u32_e32 v44, v50, v44
	v_max_u32_e32 v50, v39, v34
	v_min_u32_e32 v34, v39, v34
	v_max_u32_e32 v39, v40, v38
	v_min_u32_e32 v38, v40, v38
	v_max_u32_e32 v40, v45, v46
	v_min_u32_e32 v45, v45, v46
	v_max_u32_e32 v46, v47, v43
	v_min_u32_e32 v43, v47, v43
	v_max_u32_e32 v47, v49, v50
	v_min_u32_e32 v49, v49, v50
	v_max_u32_e32 v50, v35, v42
	v_min_u32_e32 v35, v35, v42
	v_max_u32_e32 v42, v37, v41
	v_min_u32_e32 v37, v37, v41
	v_max_u32_e32 v41, v48, v44
	v_min_u32_e32 v44, v48, v44
	v_max_u32_e32 v48, v36, v34
	v_min_u32_e32 v34, v36, v34
	v_max_u32_e32 v36, v39, v46
	v_min_u32_e32 v39, v39, v46
	v_max_u32_e32 v46, v40, v47
	v_min_u32_e32 v40, v40, v47
	v_max_u32_e32 v47, v38, v43
	v_min_u32_e32 v38, v38, v43
	v_max_u32_e32 v43, v45, v49
	v_min_u32_e32 v45, v45, v49
	v_max_u32_e32 v49, v50, v41
	v_min_u32_e32 v41, v50, v41
	v_max_u32_e32 v50, v42, v48
	v_min_u32_e32 v42, v42, v48
	v_max_u32_e32 v48, v35, v44
	v_min_u32_e32 v35, v35, v44
	v_max_u32_e32 v44, v37, v34
	v_min_u32_e32 v34, v37, v34
	v_max_u32_e32 v70, v36, v46
	v_min_u32_e32 v71, v36, v46
	v_max_u32_e32 v72, v39, v40
	v_min_u32_e32 v73, v39, v40
	v_max_u32_e32 v74, v47, v43
	v_min_u32_e32 v75, v47, v43
	v_max_u32_e32 v76, v38, v45
	v_min_u32_e32 v77, v38, v45
	v_max_u32_e32 v134, v49, v50
	v_min_u32_e32 v135, v49, v50
	v_max_u32_e32 v136, v41, v42
	v_min_u32_e32 v137, v41, v42
	v_max_u32_e32 v138, v48, v44
	v_min_u32_e32 v139, v48, v44
	v_max_u32_e32 v140, v35, v34
	v_min_u32_e32 v141, v35, v34
	global_load_dwordx4 v[46:49], v[96:97], off offset:256
	global_load_dwordx4 v[42:45], v[96:97], off offset:320
	global_load_dwordx4 v[38:41], v[96:97], off offset:384
	global_load_dwordx4 v[34:37], v[96:97], off offset:448
	ds_read_b128 v[50:53], v131 offset:34816
	ds_read_b128 v[54:57], v131 offset:34880
	s_waitcnt vmcnt(3) lgkmcnt(1)
	v_mfma_f32_16x16x32_bf16 v[50:53], v[50:53], v[46:49], 0
	ds_read_b128 v[58:61], v131 offset:39232
	ds_read_b128 v[62:65], v131 offset:43584
	ds_read_b128 v[66:69], v131 offset:47936
	s_waitcnt vmcnt(2) lgkmcnt(3)
	v_mfma_f32_16x16x32_bf16 v[50:53], v[54:57], v[42:45], v[50:53]
	ds_read_b128 v[54:57], v131 offset:34944
	ds_read_b128 v[158:161], v131 offset:52288
	ds_read_b128 v[162:165], v131 offset:56640
	s_waitcnt vmcnt(1) lgkmcnt(2)
; #define LAS __attribute__((address_space(3)))
; __device__ __forceinline__ f32x4 mfma16(bf16x8 a, bf16x8 b, f32x4 c) { return __builtin_amdgcn_mfma_f32_16x16x32_bf16(a, b, c, 0, 0, 0); }
; __device__ __forceinline__ void topk_phase(LAS unsigned char* lds, const bf16_t* qp, const bf16_t* keys, const float* SU, const float* SV, int* sel_e, float* sel_g, float* sel_su, int G, int b) {
;     ...
;             bf16x8 bq[4];
; #pragma unroll
;             for (int ks = 0; ks < 4; ++ks) bq[ks] = *(const bf16x8*)(qp + (size_t)tok * D_ + h * 256 + p * 128 + ks * 32 + fq * 8);
;             const LAS bf16_t* kb = KL + p * 128 * 136;
; #pragma unroll
;             for (int mt = 0; mt < 8; ++mt)
; #pragma unroll
;                 for (int ks = 0; ks < 4; ++ks) { const bf16x8 a = *(const LAS bf16x8*)(kb + (mt * 16 + fr) * 136 + ks * 32 + fq * 8); acc[mt] = mfma16(a, bq[ks], acc[mt]); }
	v_mfma_f32_16x16x32_bf16 v[50:53], v[54:57], v[38:41], v[50:53]
	ds_read_b128 v[54:57], v131 offset:35008
	ds_read_b128 v[166:169], v131 offset:60992
	v_mov_b32_e32 v142, v70
	s_waitcnt vmcnt(0) lgkmcnt(1)
	v_mfma_f32_16x16x32_bf16 v[50:53], v[54:57], v[34:37], v[50:53]
	ds_read_b128 v[54:57], v131 offset:39168
	v_mov_b32_e32 v143, v71
	v_mov_b32_e32 v144, v72
	s_waitcnt lgkmcnt(0)
	v_mfma_f32_16x16x32_bf16 v[54:57], v[54:57], v[46:49], 0
	s_nop 2
	v_mov_b32_e32 v145, v73
	v_mov_b32_e32 v146, v74
	v_mfma_f32_16x16x32_bf16 v[54:57], v[58:61], v[42:45], v[54:57]
	ds_read_b128 v[58:61], v131 offset:39296
	v_mov_b32_e32 v147, v75
	v_mov_b32_e32 v148, v76
	s_waitcnt lgkmcnt(0)
	v_mfma_f32_16x16x32_bf16 v[54:57], v[58:61], v[38:41], v[54:57]
	ds_read_b128 v[58:61], v131 offset:39360
	v_mov_b32_e32 v149, v77
	v_mov_b32_e32 v150, v134
	s_waitcnt lgkmcnt(0)
	v_mfma_f32_16x16x32_bf16 v[54:57], v[58:61], v[34:37], v[54:57]
	ds_read_b128 v[58:61], v131 offset:43520
	v_mov_b32_e32 v151, v135
	v_mov_b32_e32 v152, v136
	s_waitcnt lgkmcnt(0)
	v_mfma_f32_16x16x32_bf16 v[58:61], v[58:61], v[46:49], 0
	v_mov_b32_e32 v153, v137
	v_mov_b32_e32 v154, v138
	v_mov_b32_e32 v155, v139
	v_mfma_f32_16x16x32_bf16 v[58:61], v[62:65], v[42:45], v[58:61]
	ds_read_b128 v[62:65], v131 offset:43648
	v_mov_b32_e32 v156, v140
	v_mov_b32_e32 v157, v141
	s_waitcnt lgkmcnt(0)
	v_mfma_f32_16x16x32_bf16 v[58:61], v[62:65], v[38:41], v[58:61]
	ds_read_b128 v[62:65], v131 offset:43712
	v_permlane32_swap_b32_e32 v70, v142
	s_waitcnt lgkmcnt(0)
	v_mfma_f32_16x16x32_bf16 v[58:61], v[62:65], v[34:37], v[58:61]
	ds_read_b128 v[62:65], v131 offset:47872
	v_permlane32_swap_b32_e32 v71, v143
	s_waitcnt lgkmcnt(0)
	v_mfma_f32_16x16x32_bf16 v[62:65], v[62:65], v[46:49], 0
	v_permlane32_swap_b32_e32 v72, v144
	v_permlane32_swap_b32_e32 v73, v145
	v_mfma_f32_16x16x32_bf16 v[62:65], v[66:69], v[42:45], v[62:65]
	ds_read_b128 v[66:69], v131 offset:48000
	v_permlane32_swap_b32_e32 v74, v146
	s_waitcnt lgkmcnt(0)
	v_mfma_f32_16x16x32_bf16 v[62:65], v[66:69], v[38:41], v[62:65]
	ds_read_b128 v[66:69], v131 offset:48064
	v_permlane32_swap_b32_e32 v75, v147
	s_waitcnt lgkmcnt(0)
	v_mfma_f32_16x16x32_bf16 v[62:65], v[66:69], v[34:37], v[62:65]
	ds_read_b128 v[66:69], v131 offset:52224
	v_permlane32_swap_b32_e32 v76, v148
	s_waitcnt lgkmcnt(0)
	v_mfma_f32_16x16x32_bf16 v[66:69], v[66:69], v[46:49], 0
	v_permlane32_swap_b32_e32 v77, v149
	v_permlane32_swap_b32_e32 v134, v150
	v_mfma_f32_16x16x32_bf16 v[66:69], v[158:161], v[42:45], v[66:69]
	ds_read_b128 v[158:161], v131 offset:52352
	v_permlane32_swap_b32_e32 v135, v151
	s_waitcnt lgkmcnt(0)
	v_mfma_f32_16x16x32_bf16 v[66:69], v[158:161], v[38:41], v[66:69]
	ds_read_b128 v[158:161], v131 offset:52416
	v_permlane32_swap_b32_e32 v136, v152
	s_waitcnt lgkmcnt(0)
	v_mfma_f32_16x16x32_bf16 v[66:69], v[158:161], v[34:37], v[66:69]
	ds_read_b128 v[158:161], v131 offset:56576
	v_permlane32_swap_b32_e32 v137, v153
	s_waitcnt lgkmcnt(0)
	v_mfma_f32_16x16x32_bf16 v[158:161], v[158:161], v[46:49], 0
	v_permlane32_swap_b32_e32 v138, v154
	v_permlane32_swap_b32_e32 v139, v155
	v_mfma_f32_16x16x32_bf16 v[158:161], v[162:165], v[42:45], v[158:161]
	ds_read_b128 v[162:165], v131 offset:56704
	v_permlane32_swap_b32_e32 v140, v156
	s_waitcnt lgkmcnt(0)
	v_mfma_f32_16x16x32_bf16 v[158:161], v[162:165], v[38:41], v[158:161]
	ds_read_b128 v[162:165], v131 offset:56768
	v_permlane32_swap_b32_e32 v141, v157
	s_waitcnt lgkmcnt(0)
	v_mfma_f32_16x16x32_bf16 v[158:161], v[162:165], v[34:37], v[158:161]
	ds_read_b128 v[162:165], v131 offset:60928
	s_waitcnt lgkmcnt(0)
	v_mfma_f32_16x16x32_bf16 v[162:165], v[162:165], v[46:49], 0
	v_mfma_f32_16x16x32_bf16 v[162:165], v[166:169], v[42:45], v[162:165]
	ds_read_b128 v[166:169], v131 offset:61056
	s_waitcnt lgkmcnt(0)
	v_mfma_f32_16x16x32_bf16 v[162:165], v[166:169], v[38:41], v[162:165]
	ds_read_b128 v[166:169], v131 offset:61120
	s_waitcnt lgkmcnt(0)
	v_mfma_f32_16x16x32_bf16 v[162:165], v[166:169], v[34:37], v[162:165]
	ds_read_b128 v[166:169], v131 offset:65280
	s_waitcnt lgkmcnt(0)
	v_mfma_f32_16x16x32_bf16 v[46:49], v[166:169], v[46:49], 0
	ds_read_b128 v[166:169], v131 offset:65344
	s_waitcnt lgkmcnt(0)
	v_mfma_f32_16x16x32_bf16 v[42:45], v[166:169], v[42:45], v[46:49]
	s_nop 4
	ds_read_b128 v[46:49], v131 offset:65408
	s_waitcnt lgkmcnt(0)
	v_mfma_f32_16x16x32_bf16 v[38:41], v[46:49], v[38:41], v[42:45]
	s_nop 2
	ds_read_b128 v[42:45], v131 offset:65472
	s_waitcnt lgkmcnt(0)
; __device__ __forceinline__ unsigned mono(float f) { const unsigned u = __float_as_uint(f); return (u & 0x80000000u) ? ~u : (u ^ 0x80000000u); }
; __device__ __forceinline__ void topk_phase(LAS unsigned char* lds, const bf16_t* qp, const bf16_t* keys, const float* SU, const float* SV, int* sel_e, float* sel_g, float* sel_su, int G, int b) {
;     ...
;             unsigned lo16[16];
; #pragma unroll
;             for (int mt = 0; mt < 4; ++mt)
; #pragma unroll
;                 for (int r = 0; r < 4; ++r) {
;                     T[p][mt * 4 + r] = (mono(acc[mt][r]) & ~127u) | (unsigned)(127 - (mt * 16 + fq * 4 + r));
;                     lo16[mt * 4 + r] = (mono(acc[mt + 4][r]) & ~127u) | (unsigned)(127 - ((mt + 4) * 16 + fq * 4 + r));
;                 }
;             SN_SORT16(T[p]); SN_SORT16(lo16);
	v_mfma_f32_16x16x32_bf16 v[34:37], v[42:45], v[34:37], v[38:41]
	s_nop 2
	v_ashrrev_i32_e32 v38, 31, v50
	v_bitop3_b32 v38, v50, v38, v132 bitop3:0x1e
	v_and_or_b32 v38, v38, s53, v98
	v_ashrrev_i32_e32 v39, 31, v66
	v_bitop3_b32 v39, v66, v39, v132 bitop3:0x1e
	v_and_or_b32 v39, v39, s53, v99
	v_ashrrev_i32_e32 v40, 31, v51
	v_bitop3_b32 v40, v51, v40, v132 bitop3:0x1e
	v_and_or_b32 v40, v40, s53, v100
	v_ashrrev_i32_e32 v41, 31, v67
	v_bitop3_b32 v41, v67, v41, v132 bitop3:0x1e
	v_and_or_b32 v41, v41, s53, v101
	v_ashrrev_i32_e32 v42, 31, v52
	v_bitop3_b32 v42, v52, v42, v132 bitop3:0x1e
	v_and_or_b32 v42, v42, s53, v102
	v_ashrrev_i32_e32 v43, 31, v68
	v_bitop3_b32 v43, v68, v43, v132 bitop3:0x1e
	v_and_or_b32 v43, v43, s53, v103
	v_ashrrev_i32_e32 v44, 31, v53
	v_bitop3_b32 v44, v53, v44, v132 bitop3:0x1e
	v_and_or_b32 v44, v44, s53, v104
	v_ashrrev_i32_e32 v45, 31, v69
	v_bitop3_b32 v45, v69, v45, v132 bitop3:0x1e
	v_and_or_b32 v45, v45, s53, v105
	v_ashrrev_i32_e32 v46, 31, v54
	v_bitop3_b32 v46, v54, v46, v132 bitop3:0x1e
	v_and_or_b32 v46, v46, s53, v106
	v_ashrrev_i32_e32 v47, 31, v158
	v_bitop3_b32 v47, v158, v47, v132 bitop3:0x1e
	v_and_or_b32 v47, v47, s53, v107
	v_ashrrev_i32_e32 v48, 31, v55
	v_bitop3_b32 v48, v55, v48, v132 bitop3:0x1e
	v_and_or_b32 v48, v48, s53, v108
	v_ashrrev_i32_e32 v49, 31, v159
	v_bitop3_b32 v49, v159, v49, v132 bitop3:0x1e
	v_and_or_b32 v49, v49, s53, v109
	v_ashrrev_i32_e32 v50, 31, v56
	v_bitop3_b32 v50, v56, v50, v132 bitop3:0x1e
	v_and_or_b32 v50, v50, s53, v110
	v_ashrrev_i32_e32 v51, 31, v160
	v_bitop3_b32 v51, v160, v51, v132 bitop3:0x1e
	v_max_u32_e32 v160, v39, v41
	v_ashrrev_i32_e32 v52, 31, v57
	v_bitop3_b32 v52, v57, v52, v132 bitop3:0x1e
	v_min_u32_e32 v39, v39, v41
	v_ashrrev_i32_e32 v53, 31, v161
	v_bitop3_b32 v53, v161, v53, v132 bitop3:0x1e
	v_max_u32_e32 v41, v43, v45
	v_ashrrev_i32_e32 v54, 31, v58
	v_cmp_lt_i32_e32 vcc, -1, v162
	v_bitop3_b32 v54, v58, v54, v132 bitop3:0x1e
	v_min_u32_e32 v43, v43, v45
	v_cndmask_b32_e32 v55, -1, v132, vcc
	v_and_or_b32 v51, v51, s53, v111
	v_and_or_b32 v52, v52, s53, v112
	v_ashrrev_i32_e32 v56, 31, v59
	v_cmp_lt_i32_e32 vcc, -1, v163
	v_bitop3_b32 v56, v59, v56, v132 bitop3:0x1e
	v_and_or_b32 v53, v53, s53, v113
	v_cndmask_b32_e32 v57, -1, v132, vcc
	v_max_u32_e32 v45, v160, v41
	v_min_u32_e32 v41, v160, v41
	v_ashrrev_i32_e32 v58, 31, v60
	v_cmp_lt_i32_e32 vcc, -1, v164
	v_bitop3_b32 v58, v60, v58, v132 bitop3:0x1e
	v_max_u32_e32 v160, v39, v43
	v_cndmask_b32_e32 v59, -1, v132, vcc
	v_min_u32_e32 v39, v39, v43
	v_max_u32_e32 v43, v160, v41
	v_ashrrev_i32_e32 v60, 31, v61
	v_cmp_lt_i32_e32 vcc, -1, v165
	v_bitop3_b32 v60, v61, v60, v132 bitop3:0x1e
	v_min_u32_e32 v41, v160, v41
	v_cndmask_b32_e32 v61, -1, v132, vcc
	v_max_u32_e32 v160, v47, v49
	v_min_u32_e32 v47, v47, v49
	v_ashrrev_i32_e32 v66, 31, v62
	v_bitop3_b32 v62, v62, v66, v132 bitop3:0x1e
	v_max_u32_e32 v49, v51, v53
	v_ashrrev_i32_e32 v66, 31, v34
	v_bitop3_b32 v34, v34, v66, v132 bitop3:0x1e
	v_min_u32_e32 v51, v51, v53
	v_ashrrev_i32_e32 v66, 31, v63
	v_bitop3_b32 v63, v63, v66, v132 bitop3:0x1e
	v_max_u32_e32 v53, v160, v49
	v_ashrrev_i32_e32 v66, 31, v35
	v_bitop3_b32 v35, v35, v66, v132 bitop3:0x1e
	v_min_u32_e32 v49, v160, v49
	v_ashrrev_i32_e32 v66, 31, v64
	v_bitop3_b32 v64, v64, v66, v132 bitop3:0x1e
	v_max_u32_e32 v160, v47, v51
	v_ashrrev_i32_e32 v66, 31, v36
	v_bitop3_b32 v36, v36, v66, v132 bitop3:0x1e
	v_min_u32_e32 v47, v47, v51
	v_ashrrev_i32_e32 v66, 31, v65
	v_cmp_lt_i32_e32 vcc, -1, v37
	v_bitop3_b32 v65, v65, v66, v132 bitop3:0x1e
	v_max_u32_e32 v51, v160, v49
	v_cndmask_b32_e32 v66, -1, v132, vcc
	v_xor_b32_e32 v37, v66, v37
	v_max_u32_e32 v66, v38, v40
	v_min_u32_e32 v38, v38, v40
	v_max_u32_e32 v40, v42, v44
	v_min_u32_e32 v42, v42, v44
	v_max_u32_e32 v44, v66, v40
	v_min_u32_e32 v40, v66, v40
	v_max_u32_e32 v66, v38, v42
	v_min_u32_e32 v38, v38, v42
	v_max_u32_e32 v42, v66, v40
	v_min_u32_e32 v40, v66, v40
	v_max_u32_e32 v66, v46, v48
	v_min_u32_e32 v46, v46, v48
	v_max_u32_e32 v48, v50, v52
	v_min_u32_e32 v50, v50, v52
	v_max_u32_e32 v52, v66, v48
	v_min_u32_e32 v48, v66, v48
	v_max_u32_e32 v66, v46, v50
	v_min_u32_e32 v46, v46, v50
	v_max_u32_e32 v50, v66, v48
	v_min_u32_e32 v48, v66, v48
	v_min_u32_e32 v49, v160, v49
	v_max_u32_e32 v66, v44, v52
	v_min_u32_e32 v44, v44, v52
	v_max_u32_e32 v52, v40, v48
	v_max_u32_e32 v160, v45, v53
	v_min_u32_e32 v45, v45, v53
	v_max_u32_e32 v53, v41, v49
	v_xor_b32_e32 v55, v55, v162
	v_xor_b32_e32 v57, v57, v163
	v_xor_b32_e32 v59, v59, v164
	v_xor_b32_e32 v61, v61, v165
	v_min_u32_e32 v40, v40, v48
	v_max_u32_e32 v48, v52, v44
	v_min_u32_e32 v44, v52, v44
	v_max_u32_e32 v52, v42, v50
	v_min_u32_e32 v42, v42, v50
	v_max_u32_e32 v50, v38, v46
	v_min_u32_e32 v41, v41, v49
	v_max_u32_e32 v49, v53, v45
	v_min_u32_e32 v45, v53, v45
	v_max_u32_e32 v53, v43, v51
	v_min_u32_e32 v43, v43, v51
	v_max_u32_e32 v51, v39, v47
	v_and_or_b32 v54, v54, s53, v114
	v_and_or_b32 v55, v55, s53, v115
	v_and_or_b32 v56, v56, s53, v116
	v_and_or_b32 v57, v57, s53, v117
	v_and_or_b32 v58, v58, s53, v118
	v_and_or_b32 v59, v59, s53, v119
	v_and_or_b32 v60, v60, s53, v120
	v_and_or_b32 v61, v61, s53, v121
	v_min_u32_e32 v38, v38, v46
	v_max_u32_e32 v46, v50, v42
	v_min_u32_e32 v42, v50, v42
	v_min_u32_e32 v39, v39, v47
	v_max_u32_e32 v47, v51, v43
	v_min_u32_e32 v43, v51, v43
	v_max_u32_e32 v50, v52, v48
	v_min_u32_e32 v48, v52, v48
	v_max_u32_e32 v52, v46, v44
	v_min_u32_e32 v44, v46, v44
	v_max_u32_e32 v46, v42, v40
	v_min_u32_e32 v40, v42, v40
	v_max_u32_e32 v42, v54, v56
	v_min_u32_e32 v54, v54, v56
	v_max_u32_e32 v56, v58, v60
; __device__ __forceinline__ void topk_phase(LAS unsigned char* lds, const bf16_t* qp, const bf16_t* keys, const float* SU, const float* SV, int* sel_e, float* sel_g, float* sel_su, int G, int b) {
;     ...
;             SN_SORT16(T[p]); SN_SORT16(lo16);
; #pragma unroll
;             for (int i = 0; i < 16; ++i) T[p][i] = umax_(T[p][i], lo16[15 - i]);
;             SN_BITONIC16(T[p]);
	v_min_u32_e32 v58, v58, v60
	v_max_u32_e32 v51, v53, v49
	v_min_u32_e32 v49, v53, v49
	v_max_u32_e32 v53, v47, v45
	v_min_u32_e32 v45, v47, v45
	v_max_u32_e32 v47, v43, v41
	v_min_u32_e32 v41, v43, v41
	v_max_u32_e32 v43, v55, v57
	v_min_u32_e32 v55, v55, v57
	v_max_u32_e32 v57, v59, v61
	v_min_u32_e32 v59, v59, v61
	v_and_or_b32 v62, v62, s53, v122
	v_and_or_b32 v34, v34, s53, v123
	v_and_or_b32 v63, v63, s53, v124
	v_and_or_b32 v35, v35, s53, v125
	v_and_or_b32 v64, v64, s53, v126
	v_and_or_b32 v36, v36, s53, v127
	v_and_or_b32 v65, v65, s53, v128
	v_and_or_b32 v37, v37, s53, v129
	v_max_u32_e32 v60, v42, v56
	v_min_u32_e32 v42, v42, v56
	v_max_u32_e32 v56, v54, v58
	v_max_u32_e32 v61, v43, v57
	v_min_u32_e32 v43, v43, v57
	v_max_u32_e32 v57, v55, v59
	v_min_u32_e32 v54, v54, v58
	v_max_u32_e32 v58, v56, v42
	v_min_u32_e32 v42, v56, v42
	v_max_u32_e32 v56, v62, v63
	v_min_u32_e32 v62, v62, v63
	v_max_u32_e32 v63, v64, v65
	v_min_u32_e32 v64, v64, v65
	v_min_u32_e32 v55, v55, v59
	v_max_u32_e32 v59, v57, v43
	v_min_u32_e32 v43, v57, v43
	v_max_u32_e32 v57, v34, v35
	v_min_u32_e32 v34, v34, v35
	v_max_u32_e32 v35, v36, v37
	v_min_u32_e32 v36, v36, v37
	v_max_u32_e32 v65, v56, v63
	v_min_u32_e32 v56, v56, v63
	v_max_u32_e32 v63, v62, v64
	v_max_u32_e32 v37, v57, v35
	v_min_u32_e32 v35, v57, v35
	v_max_u32_e32 v57, v34, v36
	v_min_u32_e32 v62, v62, v64
	v_max_u32_e32 v64, v63, v56
	v_min_u32_e32 v56, v63, v56
	v_min_u32_e32 v34, v34, v36
	v_max_u32_e32 v36, v57, v35
	v_min_u32_e32 v35, v57, v35
	v_max_u32_e32 v63, v60, v65
	v_min_u32_e32 v60, v60, v65
	v_max_u32_e32 v65, v42, v56
	v_max_u32_e32 v57, v61, v37
	v_min_u32_e32 v37, v61, v37
	v_max_u32_e32 v61, v43, v35
	v_min_u32_e32 v42, v42, v56
	v_max_u32_e32 v56, v65, v60
	v_min_u32_e32 v60, v65, v60
	v_max_u32_e32 v65, v58, v64
	v_min_u32_e32 v58, v58, v64
	v_max_u32_e32 v64, v54, v62
	v_min_u32_e32 v35, v43, v35
	v_max_u32_e32 v43, v61, v37
	v_min_u32_e32 v37, v61, v37
	v_max_u32_e32 v61, v59, v36
	v_min_u32_e32 v36, v59, v36
	v_max_u32_e32 v59, v55, v34
	v_min_u32_e32 v54, v54, v62
	v_max_u32_e32 v62, v64, v58
	v_min_u32_e32 v34, v55, v34
	v_max_u32_e32 v55, v59, v36
	v_min_u32_e32 v58, v64, v58
	v_max_u32_e32 v64, v65, v56
	v_min_u32_e32 v56, v65, v56
	v_max_u32_e32 v65, v62, v60
	v_min_u32_e32 v60, v62, v60
	v_min_u32_e32 v36, v59, v36
	v_max_u32_e32 v59, v61, v43
	v_min_u32_e32 v43, v61, v43
	v_max_u32_e32 v61, v55, v37
	v_min_u32_e32 v37, v55, v37
	v_max_u32_e32 v62, v58, v42
	v_min_u32_e32 v42, v58, v42
	v_min_u32_e32 v58, v66, v63
	v_max_u32_e32 v67, v44, v60
	v_max_u32_e32 v55, v36, v35
	v_min_u32_e32 v35, v36, v35
	v_min_u32_e32 v36, v160, v57
	v_max_u32_e32 v161, v45, v37
	v_min_u32_e32 v44, v44, v60
	v_max_u32_e32 v60, v67, v58
	v_min_u32_e32 v58, v67, v58
	v_max_u32_e32 v67, v48, v56
	v_min_u32_e32 v48, v48, v56
	v_max_u32_e32 v56, v40, v42
	v_min_u32_e32 v37, v45, v37
	v_max_u32_e32 v45, v161, v36
	v_min_u32_e32 v36, v161, v36
	v_max_u32_e32 v161, v49, v43
	v_min_u32_e32 v43, v49, v43
	v_max_u32_e32 v49, v41, v35
	v_min_u32_e32 v40, v40, v42
	v_max_u32_e32 v42, v56, v48
	v_min_u32_e32 v48, v56, v48
	v_min_u32_e32 v35, v41, v35
	v_max_u32_e32 v41, v49, v43
	v_min_u32_e32 v43, v49, v43
	v_max_u32_e32 v56, v67, v60
	v_min_u32_e32 v60, v67, v60
	v_max_u32_e32 v67, v42, v58
	v_min_u32_e32 v42, v42, v58
	v_max_u32_e32 v58, v48, v44
	v_min_u32_e32 v44, v48, v44
	v_max_u32_e32 v48, v50, v64
	v_min_u32_e32 v50, v50, v64
	v_max_u32_e32 v64, v46, v62
	v_max_u32_e32 v49, v161, v45
	v_min_u32_e32 v45, v161, v45
	v_max_u32_e32 v161, v41, v36
	v_min_u32_e32 v36, v41, v36
	v_max_u32_e32 v41, v43, v37
	v_min_u32_e32 v37, v43, v37
	v_max_u32_e32 v43, v51, v59
	v_min_u32_e32 v51, v51, v59
	v_max_u32_e32 v59, v47, v55
	v_min_u32_e32 v46, v46, v62
	v_max_u32_e32 v62, v64, v50
	v_min_u32_e32 v50, v64, v50
	v_max_u32_e32 v64, v52, v65
	v_min_u32_e32 v52, v52, v65
	v_max_u32_e32 v65, v38, v54
	v_min_u32_e32 v47, v47, v55
	v_max_u32_e32 v55, v59, v51
	v_min_u32_e32 v51, v59, v51
	v_max_u32_e32 v59, v53, v61
	v_min_u32_e32 v53, v53, v61
	v_max_u32_e32 v61, v39, v34
	v_min_u32_e32 v38, v38, v54
	v_max_u32_e32 v54, v65, v52
	v_min_u32_e32 v52, v65, v52
	v_min_u32_e32 v34, v39, v34
	v_max_u32_e32 v39, v61, v53
	v_min_u32_e32 v53, v61, v53
	v_max_u32_e32 v65, v64, v62
	v_min_u32_e32 v62, v64, v62
	v_max_u32_e32 v64, v54, v50
	v_min_u32_e32 v50, v54, v50
	v_max_u32_e32 v54, v52, v46
	v_min_u32_e32 v46, v52, v46
	v_max_u32_e32 v61, v59, v55
	v_min_u32_e32 v55, v59, v55
	v_max_u32_e32 v59, v39, v51
	v_min_u32_e32 v39, v39, v51
	v_max_u32_e32 v51, v53, v47
	v_min_u32_e32 v47, v53, v47
	v_min_u32_e32 v52, v48, v56
	v_min_u32_e32 v68, v65, v60
	v_min_u32_e32 v69, v62, v67
	v_min_u32_e32 v96, v64, v42
	v_min_u32_e32 v97, v50, v58
	v_min_u32_e32 v158, v54, v44
	v_min_u32_e32 v159, v46, v40
	v_min_u32_e32 v53, v43, v49
	v_min_u32_e32 v162, v61, v45
	v_min_u32_e32 v163, v55, v161
	v_min_u32_e32 v164, v59, v36
	v_min_u32_e32 v165, v39, v41
	v_min_u32_e32 v166, v51, v37
	v_min_u32_e32 v167, v47, v35
	v_max3_u32 v34, v66, v63, v34
	v_max3_u32 v48, v48, v56, v167
	v_max3_u32 v35, v52, v47, v35
	v_max3_u32 v47, v65, v60, v166
	v_max3_u32 v37, v68, v51, v37
	v_max3_u32 v51, v62, v67, v165
	v_max3_u32 v39, v69, v39, v41
	v_max3_u32 v41, v64, v42, v164
	v_max3_u32 v36, v96, v59, v36
	v_max3_u32 v42, v50, v58, v163
	v_max3_u32 v50, v97, v55, v161
	v_max3_u32 v44, v54, v44, v162
	v_max3_u32 v45, v158, v61, v45
	v_max3_u32 v40, v46, v40, v53
	v_max3_u32 v43, v159, v43, v49
	v_max3_u32 v38, v38, v160, v57
	v_max_u32_e32 v46, v34, v36
	v_min_u32_e32 v34, v34, v36
	v_max_u32_e32 v36, v48, v42
	v_min_u32_e32 v42, v48, v42
	v_max_u32_e32 v48, v35, v50
	v_min_u32_e32 v35, v35, v50
	v_max_u32_e32 v49, v47, v44
	v_min_u32_e32 v44, v47, v44
	v_max_u32_e32 v47, v37, v45
	v_min_u32_e32 v37, v37, v45
	v_max_u32_e32 v45, v51, v40
	v_min_u32_e32 v40, v51, v40
	v_max_u32_e32 v50, v39, v43
	v_min_u32_e32 v39, v39, v43
	v_max_u32_e32 v43, v41, v38
	v_min_u32_e32 v38, v41, v38
	v_max_u32_e32 v41, v46, v47
	v_min_u32_e32 v46, v46, v47
	v_max_u32_e32 v47, v36, v45
	v_min_u32_e32 v36, v36, v45
	v_max_u32_e32 v45, v48, v50
	v_min_u32_e32 v48, v48, v50
	v_max_u32_e32 v50, v49, v43
	v_min_u32_e32 v43, v49, v43
	v_max_u32_e32 v49, v34, v37
	v_min_u32_e32 v34, v34, v37
	v_max_u32_e32 v37, v42, v40
	v_min_u32_e32 v40, v42, v40
	v_max_u32_e32 v42, v35, v39
	v_min_u32_e32 v35, v35, v39
	v_max_u32_e32 v39, v44, v38
	v_min_u32_e32 v38, v44, v38
	v_max_u32_e32 v44, v41, v45
	v_min_u32_e32 v41, v41, v45
	v_max_u32_e32 v45, v47, v50
	v_min_u32_e32 v47, v47, v50
	v_max_u32_e32 v50, v46, v48
	v_min_u32_e32 v46, v46, v48
	v_max_u32_e32 v48, v36, v43
	v_min_u32_e32 v36, v36, v43
	v_max_u32_e32 v43, v49, v42
	v_min_u32_e32 v42, v49, v42
	v_max_u32_e32 v49, v37, v39
	v_min_u32_e32 v37, v37, v39
	v_max_u32_e32 v39, v34, v35
	v_min_u32_e32 v34, v34, v35
	v_max_u32_e32 v35, v40, v38
	v_min_u32_e32 v38, v40, v38
	v_max_u32_e32 v40, v44, v45
	v_min_u32_e32 v44, v44, v45
	v_max_u32_e32 v45, v41, v47
	v_min_u32_e32 v41, v41, v47
	v_max_u32_e32 v47, v50, v48
	v_min_u32_e32 v48, v50, v48
	v_max_u32_e32 v50, v46, v36
	v_min_u32_e32 v36, v46, v36
	v_max_u32_e32 v46, v43, v49
	v_min_u32_e32 v43, v43, v49
	v_max_u32_e32 v49, v42, v37
	v_min_u32_e32 v37, v42, v37
	v_max_u32_e32 v42, v39, v35
	v_min_u32_e32 v35, v39, v35
	v_max_u32_e32 v39, v34, v38
	v_min_u32_e32 v34, v34, v38
	v_mov_b32_e32 v38, v40
	v_mov_b32_e32 v51, v44
	v_mov_b32_e32 v52, v45
	v_mov_b32_e32 v53, v41
	v_mov_b32_e32 v54, v47
	v_mov_b32_e32 v55, v48
	v_mov_b32_e32 v56, v50
	v_mov_b32_e32 v57, v36
	v_mov_b32_e32 v58, v46
	v_mov_b32_e32 v59, v43
	v_mov_b32_e32 v60, v49
	v_mov_b32_e32 v61, v37
	v_mov_b32_e32 v62, v42
	v_mov_b32_e32 v63, v35
	v_mov_b32_e32 v64, v39
	v_mov_b32_e32 v65, v34
	v_permlane16_swap_b32_e32 v40, v38
	v_permlane16_swap_b32_e32 v44, v51
	v_permlane16_swap_b32_e32 v45, v52
	v_permlane16_swap_b32_e32 v41, v53
	v_permlane16_swap_b32_e32 v47, v54
	v_permlane16_swap_b32_e32 v48, v55
	v_permlane16_swap_b32_e32 v50, v56
	v_permlane16_swap_b32_e32 v36, v57
	v_permlane16_swap_b32_e32 v46, v58
	v_permlane16_swap_b32_e32 v43, v59
	v_permlane16_swap_b32_e32 v49, v60
	v_permlane16_swap_b32_e32 v37, v61
	v_permlane16_swap_b32_e32 v42, v62
	v_permlane16_swap_b32_e32 v35, v63
	v_permlane16_swap_b32_e32 v39, v64
	v_permlane16_swap_b32_e32 v34, v65
	v_max_u32_e32 v40, v40, v65
	v_max_u32_e32 v44, v44, v64
	v_max_u32_e32 v45, v45, v63
	v_max_u32_e32 v41, v41, v62
	v_max_u32_e32 v47, v47, v61
	v_max_u32_e32 v48, v48, v60
	v_max_u32_e32 v50, v50, v59
	v_max_u32_e32 v36, v36, v58
	v_max_u32_e32 v46, v46, v57
	v_max_u32_e32 v43, v43, v56
	v_max_u32_e32 v49, v49, v55
	v_max_u32_e32 v37, v37, v54
	v_max_u32_e32 v42, v42, v53
	v_max_u32_e32 v35, v35, v52
	v_max_u32_e32 v39, v39, v51
	v_max_u32_e32 v34, v34, v38
	v_max_u32_e32 v38, v40, v46
	v_min_u32_e32 v40, v40, v46
	v_max_u32_e32 v46, v44, v43
	v_min_u32_e32 v43, v44, v43
	v_max_u32_e32 v44, v45, v49
	v_min_u32_e32 v45, v45, v49
	v_max_u32_e32 v49, v41, v37
	v_min_u32_e32 v37, v41, v37
	v_max_u32_e32 v41, v47, v42
	v_min_u32_e32 v42, v47, v42
	v_max_u32_e32 v47, v48, v35
	v_min_u32_e32 v35, v48, v35
	v_max_u32_e32 v48, v50, v39
	v_min_u32_e32 v39, v50, v39
	v_max_u32_e32 v50, v36, v34
	v_min_u32_e32 v34, v36, v34
	v_max_u32_e32 v36, v38, v41
	v_min_u32_e32 v38, v38, v41
	v_max_u32_e32 v41, v46, v47
	v_min_u32_e32 v46, v46, v47
	v_max_u32_e32 v47, v44, v48
	v_min_u32_e32 v44, v44, v48
	v_max_u32_e32 v48, v49, v50
	v_min_u32_e32 v49, v49, v50
	v_max_u32_e32 v50, v40, v42
	v_min_u32_e32 v40, v40, v42
	v_max_u32_e32 v42, v43, v35
	v_min_u32_e32 v35, v43, v35
	v_max_u32_e32 v43, v45, v39
	v_min_u32_e32 v39, v45, v39
	v_max_u32_e32 v45, v37, v34
	v_min_u32_e32 v34, v37, v34
	v_max_u32_e32 v37, v36, v47
	v_min_u32_e32 v47, v36, v47
	v_max_u32_e32 v51, v41, v48
	v_min_u32_e32 v41, v41, v48
	v_max_u32_e32 v48, v38, v44
	v_min_u32_e32 v44, v38, v44
	v_max_u32_e32 v52, v46, v49
	v_min_u32_e32 v46, v46, v49
	v_max_u32_e32 v49, v50, v43
	v_min_u32_e32 v50, v50, v43
	v_max_u32_e32 v53, v42, v45
	v_min_u32_e32 v55, v42, v45
	v_max_u32_e32 v58, v40, v39
	v_min_u32_e32 v59, v40, v39
	v_max_u32_e32 v60, v35, v34
	v_min_u32_e32 v34, v35, v34
	v_max_u32_e32 v36, v37, v51
	v_min_u32_e32 v37, v37, v51
	v_max_u32_e32 v38, v47, v41
	v_min_u32_e32 v39, v47, v41
	v_max_u32_e32 v40, v48, v52
	v_min_u32_e32 v41, v48, v52
; __device__ __forceinline__ unsigned mono(float f) { const unsigned u = __float_as_uint(f); return (u & 0x80000000u) ? ~u : (u ^ 0x80000000u); }
; __device__ __forceinline__ float unmono(unsigned u) { return __uint_as_float((u & 0x80000000u) ? (u ^ 0x80000000u) : ~u); }
; __device__ __forceinline__ void topk_phase(LAS unsigned char* lds, const bf16_t* qp, const bf16_t* keys, const float* SU, const float* SV, int* sel_e, float* sel_g, float* sel_su, int G, int b) {
;     ...
;         float v1[16], v2[16];
; #pragma unroll
;         for (int i = 0; i < 16; ++i) { v1[i] = unmono(T[0][i] & ~127u); v2[i] = unmono(T[1][i] & ~127u); }
;         unsigned ck[16];
; #pragma unroll
;         for (int sidx = 0; sidx < 13; ++sidx) {
;             unsigned keyk[4];
; #pragma unroll
;             for (int k = 0; k < 4; ++k) {
;                 const int c = 4 * sidx + k;
;                 if (c < 50) { const int ci = cand_i(c), cj = cand_j(c); keyk[k] = (mono(v1[ci] + v2[cj]) & ~255u) | (unsigned)(255 - (ci * 16 + cj)); }
;                 else keyk[k] = 0u;
;             }
;             ck[sidx] = fq == 0 ? keyk[0] : fq == 1 ? keyk[1] : fq == 2 ? keyk[2] : keyk[3];
	v_max_u32_e32 v42, v44, v46
	v_min_u32_e32 v43, v44, v46
	v_max_u32_e32 v44, v49, v53
	v_min_u32_e32 v45, v49, v53
	v_max_u32_e32 v54, v50, v55
	v_min_u32_e32 v56, v50, v55
	v_max_u32_e32 v57, v58, v60
	v_min_u32_e32 v66, v58, v60
	v_max_u32_e32 v67, v59, v34
	v_min_u32_e32 v68, v59, v34
	v_mov_b32_e32 v69, v36
	v_mov_b32_e32 v158, v37
	v_mov_b32_e32 v159, v38
	v_mov_b32_e32 v160, v39
	v_mov_b32_e32 v161, v40
	v_mov_b32_e32 v162, v41
	v_mov_b32_e32 v163, v42
	v_mov_b32_e32 v97, v43
	v_mov_b32_e32 v53, v44
	v_mov_b32_e32 v52, v45
	v_mov_b32_e32 v51, v54
	v_mov_b32_e32 v50, v56
	v_mov_b32_e32 v49, v57
	v_mov_b32_e32 v48, v66
	v_mov_b32_e32 v47, v67
	v_mov_b32_e32 v46, v68
	v_permlane32_swap_b32_e32 v36, v69
	v_permlane32_swap_b32_e32 v37, v158
	v_permlane32_swap_b32_e32 v38, v159
	v_permlane32_swap_b32_e32 v39, v160
	v_permlane32_swap_b32_e32 v40, v161
	v_permlane32_swap_b32_e32 v41, v162
	v_permlane32_swap_b32_e32 v42, v163
	v_permlane32_swap_b32_e32 v43, v97
	v_permlane32_swap_b32_e32 v44, v53
	v_permlane32_swap_b32_e32 v45, v52
	v_permlane32_swap_b32_e32 v54, v51
	v_permlane32_swap_b32_e32 v56, v50
	v_permlane32_swap_b32_e32 v57, v49
	v_permlane32_swap_b32_e32 v66, v48
	v_permlane32_swap_b32_e32 v67, v47
	v_permlane32_swap_b32_e32 v68, v46
	v_max_u32_e32 v59, v70, v157
	v_max_u32_e32 v60, v71, v156
	v_max_u32_e32 v61, v72, v155
	v_max_u32_e32 v62, v73, v154
	v_max_u32_e32 v63, v74, v153
	v_max_u32_e32 v64, v75, v152
	v_max_u32_e32 v65, v76, v151
	v_max_u32_e32 v70, v77, v150
	v_max_u32_e32 v71, v134, v149
	v_max_u32_e32 v72, v135, v148
	v_max_u32_e32 v73, v136, v147
	v_max_u32_e32 v74, v137, v146
	v_max_u32_e32 v75, v138, v145
	v_max_u32_e32 v76, v139, v144
	v_max_u32_e32 v77, v140, v143
	v_max_u32_e32 v96, v141, v142
	v_max_u32_e32 v55, v59, v71
	v_max_u32_e32 v135, v60, v72
	v_max_u32_e32 v136, v61, v73
	v_max_u32_e32 v137, v62, v74
	v_max_u32_e32 v138, v63, v75
	v_max_u32_e32 v139, v64, v76
	v_max_u32_e32 v140, v65, v77
	v_max_u32_e32 v141, v70, v96
	v_max_u32_e32 v46, v36, v46
	v_max_u32_e32 v47, v37, v47
	v_max_u32_e32 v48, v38, v48
	v_max_u32_e32 v49, v39, v49
	v_max_u32_e32 v50, v40, v50
	v_max_u32_e32 v51, v41, v51
	v_max_u32_e32 v52, v42, v52
	v_max_u32_e32 v53, v43, v53
	v_max_u32_e32 v97, v44, v97
	v_max_u32_e32 v134, v45, v163
	v_max_u32_e32 v143, v54, v162
	v_max_u32_e32 v149, v56, v161
	v_max_u32_e32 v150, v57, v160
	v_max_u32_e32 v151, v66, v159
	v_max_u32_e32 v152, v67, v158
	v_max_u32_e32 v153, v68, v69
	v_max_u32_e32 v58, v55, v138
	v_max_u32_e32 v144, v135, v139
	v_max_u32_e32 v145, v136, v140
	v_max_u32_e32 v146, v137, v141
	v_max_u32_e32 v36, v46, v97
	v_max_u32_e32 v37, v47, v134
	v_max_u32_e32 v42, v48, v143
	v_max_u32_e32 v43, v49, v149
	v_max_u32_e32 v44, v50, v150
	v_max_u32_e32 v45, v51, v151
	v_max_u32_e32 v69, v52, v152
	v_max_u32_e32 v147, v53, v153
	v_max_u32_e32 v35, v58, v145
	v_max_u32_e32 v142, v144, v146
	v_max_u32_e32 v38, v36, v44
	v_max_u32_e32 v39, v37, v45
	v_max_u32_e32 v40, v42, v69
	v_max_u32_e32 v41, v43, v147
	v_max_u32_e32 v34, v35, v142
	v_max_u32_e32 v54, v38, v40
	v_min_u32_e32 v56, v38, v40
	v_max_u32_e32 v40, v39, v41
	v_min_u32_e32 v41, v39, v41
	v_min_u32_e32 v39, v54, v40
	v_cmp_lt_i32_e32 vcc, -1, v34
	v_max_u32_e32 v38, v54, v40
	v_max_u32_e32 v40, v56, v41
	v_cndmask_b32_e64 v54, v132, -1, vcc
	v_cmp_lt_i32_e32 vcc, -1, v39
	v_min_u32_e32 v41, v56, v41
	v_and_b32_e32 v56, 0xffffff80, v39
	v_cndmask_b32_e64 v66, v132, -1, vcc
	v_cmp_lt_i32_e32 vcc, -1, v38
	v_and_b32_e32 v57, 0xffffff80, v38
	v_xor_b32_e32 v67, v66, v56
	v_cndmask_b32_e64 v68, v132, -1, vcc
	v_cmp_lt_i32_e32 vcc, -1, v41
	v_xor_b32_e32 v66, v68, v57
	v_bitop3_b32 v54, v54, v34, s53 bitop3:0x78
	v_cndmask_b32_e64 v57, v132, -1, vcc
	v_cmp_lt_i32_e32 vcc, -1, v40
	v_and_b32_e32 v56, 0xffffff80, v41
	v_and_b32_e32 v68, 0xffffff80, v40
	v_cndmask_b32_e64 v148, v132, -1, vcc
	v_xor_b32_e32 v57, v57, v56
	v_xor_b32_e32 v56, v148, v68
	v_add_f32_e32 v68, v66, v54
	v_cmp_lt_i32_e32 vcc, -1, v68
	s_nop 1
	v_cndmask_b32_e32 v148, -1, v132, vcc
	v_bitop3_b32 v68, v148, s0, v68 bitop3:0xde
	v_cmp_lt_i32_e32 vcc, 0, v1
	s_and_saveexec_b64 s[0:1], vcc
	s_cbranch_execz .LBB0_665
	v_cmp_ne_u32_e32 vcc, 1, v1
	s_and_saveexec_b64 s[4:5], vcc
	s_xor_b64 s[4:5], exec, s[4:5]
	s_cbranch_execz .LBB0_662
	v_pk_add_f32 v[154:155], v[54:55], v[56:57] op_sel_hi:[0,1]
	v_cmp_lt_i32_e32 vcc, -1, v155
	v_and_b32_e32 v148, 0xffffff00, v155
	s_movk_i32 s6, 0xfc
	v_cndmask_b32_e32 v68, v133, v132, vcc
	v_cmp_lt_i32_e32 vcc, -1, v154
	v_bitop3_b32 v68, v68, s6, v148 bitop3:0xde
	v_and_b32_e32 v154, 0xffffff00, v154
	v_cndmask_b32_e32 v148, v133, v132, vcc
	s_movk_i32 s6, 0xfd
	v_bitop3_b32 v148, v148, s6, v154 bitop3:0xde
	v_cndmask_b32_e64 v68, v68, v148, s[38:39]
